# P6-hosted conversion share enlarged: items [25088,39168) on the P6-idle workgroups (was [28160,39168))
# speedup vs baseline: 1.0001x; 1.0001x over previous
; #define LAS __attribute__((address_space(3)))
; #define LAS __attribute__((address_space(3)))
;     LAS unsigned* scr = (LAS unsigned*)(lds + wave * 16384);
;     WItem d0, d1; WRegs R0, R1;
;     constexpr int KB_ = DM / 32;
;     constexpr int NALL = EARLY ? KB_ * (INW / 128) : KB_ * (DM / 128) + KB_ * (CW / 128) + KB_ * (2 * CW / 128) + (CW / 32) * (DM / 128) + KB_ * (DFF2 / 128) + (DFF / 32) * (DM / 128);
;     const int hi_all = it_hi < NALL ? it_hi : NALL, total = hi_all - it_lo, nwgs = NGW / NWAVES, chunk = (((total + nwgs - 1) / nwgs) + NWAVES - 1) / NWAVES * NWAVES;
;     int it = it_lo + (gw / NWAVES) * chunk + (gw % NWAVES); const int wend0 = it_lo + (gw / NWAVES + 1) * chunk, wend = wend0 < hi_all ? wend0 : hi_all;
; __global__ void __launch_bounds__(NWAVES * 64, 2) mk_fwd(Args args) {
;     ...
;         const int NCONV = (CONV_OVERLAP && G >= 128) ? 51 : 0;
;         if (bx < NCONV) convert_weights<false, true>(P, lds, bx * NWAVES + wave, NCONV * NWAVES, wave, lane, 0, (CONV_OVERLAP && G >= 192) ? LATE_SPLIT : 0x7fffffff);
;         else {
;             sb_phase(lds, PROJ, (bf16*)(ws + WS_MIX), (const float*)(ws + WS_RSB), P.sbo_norm, bx - NCONV, G - NCONV, tid);
;             ret_out_phase(lds, PROJ, (bf16*)(ws + WS_MIX), (const bf16*)(ws + WS_ST), P.ret_norm, bx - NCONV, G - NCONV, tid);
;         }
;         if (NCONV == 0) convert_weights<false>(P, lds, gw, NGW, wave, lane);
.LBB0_519:
	s_mov_b32 s98, 0
	s_mov_b32 s99, 0
	s_mov_b32 s100, s80
	s_mov_b32 s101, s56
	s_mov_b32 s0, 0x9900
	s_cmp_eq_u32 s80, 0x100
	s_cselect_b32 s1, 1, 0
	s_cmp_gt_i32 s75, 6
	s_cselect_b32 s1, s1, 0
	s_cmp_lg_u32 s1, 0
	s_cselect_b32 s0, 0x6200, s0
	v_writelane_b32 v255, s0, 2
	s_mov_b32 s0, 0
	v_writelane_b32 v255, s0, 3

; #define LAS __attribute__((address_space(3)))
; #define LAS __attribute__((address_space(3)))
;     LAS unsigned* scr = (LAS unsigned*)(lds + wave * 16384);
;     WItem d0, d1; WRegs R0, R1;
;     constexpr int KB_ = DM / 32;
;     constexpr int NALL = EARLY ? KB_ * (INW / 128) : KB_ * (DM / 128) + KB_ * (CW / 128) + KB_ * (2 * CW / 128) + (CW / 32) * (DM / 128) + KB_ * (DFF2 / 128) + (DFF / 32) * (DM / 128);
;     const int hi_all = it_hi < NALL ? it_hi : NALL, total = hi_all - it_lo, nwgs = NGW / NWAVES, chunk = (((total + nwgs - 1) / nwgs) + NWAVES - 1) / NWAVES * NWAVES;
;     int it = it_lo + (gw / NWAVES) * chunk + (gw % NWAVES); const int wend0 = it_lo + (gw / NWAVES + 1) * chunk, wend = wend0 < hi_all ? wend0 : hi_all;
; __global__ void __launch_bounds__(NWAVES * 64, 2) mk_fwd(Args args) {
;     ...
;         { pg8::Gemm g{(const bf16*)(ws + WS_MB), (const bf16*)(ws + WS_WQKV) + (size_t)CW * DM, BATCH * NMEM, 2 * CW, DM, DM}; pg8::StaticOrder S; S.init(BATCH * NMEM, 2 * CW, G, (bx + G / 2) % G);
;           pg8::EpiScaleF32 E{(float*)(ws + WS_CKV), 2 * CW, (const float*)(ws + WS_SSQM)};
;           pg8::gemm_phase<pg8::EpiScaleF32, pg8::StaticOrder, true, true>(lds, g, S, E); }
;         if (CONV_OVERLAP && G >= 192 && bx >= G / 2 + 8) { __syncthreads(); convert_weights<false, true>(P, lds, (bx - (G / 2 + 8)) * NWAVES + wave, (G - (G / 2 + 8)) * NWAVES, wave, lane, LATE_SPLIT, 0x7fffffff); }
.LBB0_925:
	s_cmpk_lt_i32 s2, 0x88
	s_cbranch_scc1 .Lp6_hook_done
	s_cmp_lg_u32 s80, 0x100
	s_cbranch_scc1 .Lp6_hook_done
	s_cmp_gt_i32 s74, 4
	s_cbranch_scc1 .Lp6_hook_done
	s_cmp_lt_i32 s75, 7
	s_cbranch_scc1 .Lp6_hook_done
	v_writelane_b32 v255, s8, 8
	v_writelane_b32 v255, s9, 9
	v_writelane_b32 v255, s12, 10
	v_writelane_b32 v255, s16, 11
	v_writelane_b32 v255, s18, 12
	v_writelane_b32 v255, s19, 13
	v_writelane_b32 v255, s20, 14
	v_writelane_b32 v255, s21, 15
	v_writelane_b32 v255, s23, 16
	v_writelane_b32 v255, s24, 17
	v_writelane_b32 v255, s26, 18
	v_writelane_b32 v255, s34, 19
	v_readlane_b32 s70, v254, 0
	v_readlane_b32 s71, v254, 1
	v_and_b32_e32 v1, 63, v0
	v_readfirstlane_b32 s101, v0
	s_sub_u32 s100, s2, 0x88
	s_lshl_b32 s100, s100, 3
	s_sub_u32 s70, s70, 0xc0
	s_subb_u32 s71, s71, 0
	s_lshr_b32 s101, s101, 6
	s_add_u32 s101, s101, s100
	s_mov_b32 s100, 120
	s_mov_b32 s0, 0x3700
	v_writelane_b32 v255, s0, 2
	s_mov_b32 s0, 0x6200
	v_writelane_b32 v255, s0, 3
	s_mov_b32 s98, 1
	s_mov_b32 s99, 1
	s_mov_b64 s[4:5], -1
	s_branch .Lp4_conv_entry
